# v43 + the five GEMM K-loop heads aligned to 64 bytes (.p2align 6)
# baseline (speedup 1.0000x reference)
; #define PG8_STAGE(bufoff, gbase, voff) do { _Pragma("unroll") for (int _i = 0; _i < 2; ++_i) \
;         __builtin_amdgcn_global_load_lds((const unsigned*)((const char*)(gbase) + (voff)[_i]), (PG8_LAS unsigned*)(lds + (bufoff) + ldsw + _i * 8192), 16, 0, 0); } while (0)
; #define PG8_LDA(dst, b, h) do { _Pragma("unroll") for (int m = 0; m < 4; ++m) _Pragma("unroll") for (int k = 0; k < 2; ++k) dst[m][k] = *(const PG8_LAS bf16x8*)(lds + PG8_SA(b, h) + aoff + m * 2048 + k * 1024); } while (0)
; #define PG8_LDB(dst, b, h) do { _Pragma("unroll") for (int n = 0; n < 2; ++n) _Pragma("unroll") for (int k = 0; k < 2; ++k) dst[n][k] = *(const PG8_LAS bf16x8*)(lds + PG8_SB(b, h) + boff + n * 2048 + k * 1024); } while (0)
; #define PG8_WAIT_V(n) asm volatile("s_waitcnt vmcnt(" #n ")" ::: "memory")
; #define PG8_WAIT_L(n) asm volatile("s_waitcnt lgkmcnt(" #n ")" ::: "memory")
; template <class Epi, class Sched, bool ALIGN_EPI = false, bool SP2 = false>
; __device__ __forceinline__ void gemm_phase(PG8_LAS unsigned char* lds, const Gemm g, const Sched& S, const Epi& E) {
;     ...
;             PG8_LDB(B0, 0, 0); PG8_LDB(B1, 0, 1); PG8_SCHED; PG8_LDA(At, 0, 0); PG8_STAGE(PG8_SA(1, 1), a1 + hstep, voffA);
;     ...
;             if (PROBE_KIND == 18 && t == 0 && ui > 0 && g.probe) { const unsigned long long tq_ = __builtin_amdgcn_s_memrealtime(); PG8_WAIT_V(8); pg8_probe_acc += (unsigned)(__builtin_amdgcn_s_memrealtime() - tq_); }
;     ...
;             PG8_WAIT_V(8); PG8_WAIT_L(0); PG8_BAR; PG8_MMA(0, 0, At, B0); PG8_MMA(0, 1, At, B1); PG8_BAR; PG8_SCHED;
;             PG8_LDA(At, 0, 1); PG8_STAGE(PG8_SB(0, 0), b2, voffB); PG8_STAGE(PG8_SB(0, 1), b2 + hstep, voffB); PG8_STAGE(PG8_SA(0, 0), a2, voffA);
;             PG8_WAIT_V(8); PG8_WAIT_L(0); PG8_BAR; if (cur.half == 0) { PG8_MMA(1, 0, At, B0); PG8_MMA(1, 1, At, B1); } PG8_BAR; PG8_SCHED;
;             PG8_LDB(B0, 1, 0); PG8_LDB(B1, 1, 1); PG8_SCHED; PG8_LDA(At, 1, 0); PG8_STAGE(PG8_SA(0, 1), a2 + hstep, voffA);
;             PG8_WAIT_V(8); PG8_WAIT_L(0); PG8_BAR; PG8_MMA(0, 0, At, B0); PG8_MMA(0, 1, At, B1); PG8_BAR; PG8_SCHED;
;             PG8_LDA(At, 1, 1); PG8_STAGE(PG8_SB(1, 0), b3, voffB); PG8_STAGE(PG8_SB(1, 1), b3 + hstep, voffB); PG8_STAGE(PG8_SA(1, 0), a3, voffA);
;             PG8_WAIT_V(8); PG8_WAIT_L(0); PG8_BAR; if (cur.half == 0) { PG8_MMA(1, 0, At, B0); PG8_MMA(1, 1, At, B1); } PG8_BAR; PG8_SCHED;
.Lpj_ip_2:
	s_waitcnt lgkmcnt(0)
	s_barrier
	s_setprio 1
	s_waitcnt lgkmcnt(0)
	v_mfma_f32_16x16x32_bf16 v[64:67], v[132:135], v[182:185], 0
	v_mfma_f32_16x16x32_bf16 v[60:63], v[140:143], v[182:185], 0
	v_mfma_f32_16x16x32_bf16 v[48:51], v[132:135], v[190:193], 0
	v_mfma_f32_16x16x32_bf16 v[44:47], v[140:143], v[190:193], 0
	v_mfma_f32_16x16x32_bf16 v[32:35], v[132:135], v[198:201], 0
	v_mfma_f32_16x16x32_bf16 v[28:31], v[140:143], v[198:201], 0
	v_mfma_f32_16x16x32_bf16 v[16:19], v[132:135], v[212:215], 0
	v_mfma_f32_16x16x32_bf16 v[12:15], v[140:143], v[212:215], 0
	v_mfma_f32_16x16x32_bf16 v[64:67], v[136:139], v[186:189], v[64:67]
	v_mfma_f32_16x16x32_bf16 v[60:63], v[144:147], v[186:189], v[60:63]
	v_mfma_f32_16x16x32_bf16 v[48:51], v[136:139], v[194:197], v[48:51]
	v_mfma_f32_16x16x32_bf16 v[44:47], v[144:147], v[194:197], v[44:47]
	v_mfma_f32_16x16x32_bf16 v[32:35], v[136:139], v[208:211], v[32:35]
	v_mfma_f32_16x16x32_bf16 v[28:31], v[144:147], v[208:211], v[28:31]
	v_mfma_f32_16x16x32_bf16 v[16:19], v[136:139], v[216:219], v[16:19]
	v_mfma_f32_16x16x32_bf16 v[12:15], v[144:147], v[216:219], v[12:15]
	s_setprio 0
	s_setprio 1
	v_mfma_f32_16x16x32_bf16 v[56:59], v[148:151], v[182:185], 0
	v_mfma_f32_16x16x32_bf16 v[52:55], v[156:159], v[182:185], 0
	v_mfma_f32_16x16x32_bf16 v[40:43], v[148:151], v[190:193], 0
	v_mfma_f32_16x16x32_bf16 v[36:39], v[156:159], v[190:193], 0
	v_mfma_f32_16x16x32_bf16 v[24:27], v[148:151], v[198:201], 0
	v_mfma_f32_16x16x32_bf16 v[20:23], v[156:159], v[198:201], 0
	v_mfma_f32_16x16x32_bf16 v[8:11], v[148:151], v[212:215], 0
	v_mfma_f32_16x16x32_bf16 v[4:7], v[156:159], v[212:215], 0
	v_mfma_f32_16x16x32_bf16 v[56:59], v[152:155], v[186:189], v[56:59]
	v_mfma_f32_16x16x32_bf16 v[52:55], v[160:163], v[186:189], v[52:55]
	v_mfma_f32_16x16x32_bf16 v[40:43], v[152:155], v[194:197], v[40:43]
	v_mfma_f32_16x16x32_bf16 v[36:39], v[160:163], v[194:197], v[36:39]
	v_mfma_f32_16x16x32_bf16 v[24:27], v[152:155], v[208:211], v[24:27]
	v_mfma_f32_16x16x32_bf16 v[20:23], v[160:163], v[208:211], v[20:23]
	v_mfma_f32_16x16x32_bf16 v[8:11], v[152:155], v[216:219], v[8:11]
	v_mfma_f32_16x16x32_bf16 v[4:7], v[160:163], v[216:219], v[4:7]
	s_setprio 0
	s_barrier
	s_add_i32 s61, 0, 0x18000
	v_add_u32_e32 v2, s61, v203
	s_add_i32 s63, 0, 0x1c000
	ds_read_b128 v[132:135], v2
	ds_read_b128 v[136:139], v2 offset:1024
	ds_read_b128 v[140:143], v2 offset:2048
	ds_read_b128 v[144:147], v2 offset:3072
	v_add_u32_e32 v2, s63, v203
	ds_read_b128 v[148:151], v2
	ds_read_b128 v[152:155], v2 offset:1024
	ds_read_b128 v[156:159], v2 offset:2048
	ds_read_b128 v[160:163], v2 offset:3072
	s_add_u32 s10, s10, 0x40000
	s_addc_u32 s11, s11, 0
	s_mov_b32 m0, s31
	v_lshl_add_u64 v[236:237], s[10:11], 0, v[164:165]
	ds_read_b128 v[182:185], v206 offset:32768
	ds_read_b128 v[186:189], v206 offset:33792
	ds_read_b128 v[190:193], v206 offset:34816
	ds_read_b128 v[194:197], v206 offset:35840
	ds_read_b128 v[198:201], v206 offset:36864
	ds_read_b128 v[208:211], v206 offset:37888
	ds_read_b128 v[212:215], v206 offset:38912
	ds_read_b128 v[216:219], v206 offset:39936
	global_load_lds_dwordx4 v[236:237], off
	v_lshl_add_u64 v[236:237], s[10:11], 0, v[168:169]
	s_mov_b32 m0, s34
	s_nop 0
	global_load_lds_dwordx4 v[236:237], off
	s_waitcnt vmcnt(8)
	s_waitcnt lgkmcnt(0)
	s_barrier
	s_setprio 1
	s_waitcnt lgkmcnt(0)
	v_mfma_f32_16x16x32_bf16 v[128:131], v[132:135], v[182:185], v[128:131]
	v_mfma_f32_16x16x32_bf16 v[124:127], v[140:143], v[182:185], v[124:127]
	v_mfma_f32_16x16x32_bf16 v[112:115], v[132:135], v[190:193], v[112:115]
	v_mfma_f32_16x16x32_bf16 v[108:111], v[140:143], v[190:193], v[108:111]
	v_mfma_f32_16x16x32_bf16 v[96:99], v[132:135], v[198:201], v[96:99]
	v_mfma_f32_16x16x32_bf16 v[92:95], v[140:143], v[198:201], v[92:95]
	v_mfma_f32_16x16x32_bf16 v[80:83], v[132:135], v[212:215], v[80:83]
	v_mfma_f32_16x16x32_bf16 v[76:79], v[140:143], v[212:215], v[76:79]
	v_mfma_f32_16x16x32_bf16 v[128:131], v[136:139], v[186:189], v[128:131]
	v_mfma_f32_16x16x32_bf16 v[124:127], v[144:147], v[186:189], v[124:127]
	v_mfma_f32_16x16x32_bf16 v[112:115], v[136:139], v[194:197], v[112:115]
	v_mfma_f32_16x16x32_bf16 v[108:111], v[144:147], v[194:197], v[108:111]
	v_mfma_f32_16x16x32_bf16 v[96:99], v[136:139], v[208:211], v[96:99]
	v_mfma_f32_16x16x32_bf16 v[92:95], v[144:147], v[208:211], v[92:95]
	v_mfma_f32_16x16x32_bf16 v[80:83], v[136:139], v[216:219], v[80:83]
	v_mfma_f32_16x16x32_bf16 v[76:79], v[144:147], v[216:219], v[76:79]
	s_setprio 0
	s_setprio 1
	v_mfma_f32_16x16x32_bf16 v[120:123], v[148:151], v[182:185], v[120:123]
	v_mfma_f32_16x16x32_bf16 v[116:119], v[156:159], v[182:185], v[116:119]
	v_mfma_f32_16x16x32_bf16 v[104:107], v[148:151], v[190:193], v[104:107]
	v_mfma_f32_16x16x32_bf16 v[100:103], v[156:159], v[190:193], v[100:103]
	v_mfma_f32_16x16x32_bf16 v[88:91], v[148:151], v[198:201], v[88:91]
	v_mfma_f32_16x16x32_bf16 v[84:87], v[156:159], v[198:201], v[84:87]
	v_mfma_f32_16x16x32_bf16 v[72:75], v[148:151], v[212:215], v[72:75]
	v_mfma_f32_16x16x32_bf16 v[68:71], v[156:159], v[212:215], v[68:71]
	v_mfma_f32_16x16x32_bf16 v[120:123], v[152:155], v[186:189], v[120:123]
	v_mfma_f32_16x16x32_bf16 v[116:119], v[160:163], v[186:189], v[116:119]
	v_mfma_f32_16x16x32_bf16 v[104:107], v[152:155], v[194:197], v[104:107]
	v_mfma_f32_16x16x32_bf16 v[100:103], v[160:163], v[194:197], v[100:103]
	v_mfma_f32_16x16x32_bf16 v[88:91], v[152:155], v[208:211], v[88:91]
	v_mfma_f32_16x16x32_bf16 v[84:87], v[160:163], v[208:211], v[84:87]
	v_mfma_f32_16x16x32_bf16 v[72:75], v[152:155], v[216:219], v[72:75]
	v_mfma_f32_16x16x32_bf16 v[68:71], v[160:163], v[216:219], v[68:71]
	s_setprio 0
	s_barrier
; #define PG8_STAGE(bufoff, gbase, voff) do { _Pragma("unroll") for (int _i = 0; _i < 2; ++_i) \
;         __builtin_amdgcn_global_load_lds((const unsigned*)((const char*)(gbase) + (voff)[_i]), (PG8_LAS unsigned*)(lds + (bufoff) + ldsw + _i * 8192), 16, 0, 0); } while (0)
; #define PG8_LDA(dst, b, h) do { _Pragma("unroll") for (int m = 0; m < 4; ++m) _Pragma("unroll") for (int k = 0; k < 2; ++k) dst[m][k] = *(const PG8_LAS bf16x8*)(lds + PG8_SA(b, h) + aoff + m * 2048 + k * 1024); } while (0)
; #define PG8_LDB(dst, b, h) do { _Pragma("unroll") for (int n = 0; n < 2; ++n) _Pragma("unroll") for (int k = 0; k < 2; ++k) dst[n][k] = *(const PG8_LAS bf16x8*)(lds + PG8_SB(b, h) + boff + n * 2048 + k * 1024); } while (0)
; #define PG8_WAIT_V(n) asm volatile("s_waitcnt vmcnt(" #n ")" ::: "memory")
; #define PG8_WAIT_L(n) asm volatile("s_waitcnt lgkmcnt(" #n ")" ::: "memory")
; template <class Epi, class Sched, bool ALIGN_EPI = false, bool SP2 = false>
; __device__ __forceinline__ void gemm_phase(PG8_LAS unsigned char* lds, const Gemm g, const Sched& S, const Epi& E) {
;     ...
;             PG8_LDB(B0, 0, 0); PG8_LDB(B1, 0, 1); PG8_SCHED; PG8_LDA(At, 0, 0); PG8_STAGE(PG8_SA(1, 1), a1 + hstep, voffA);
;     ...
;             if (PROBE_KIND == 18 && t == 0 && ui > 0 && g.probe) { const unsigned long long tq_ = __builtin_amdgcn_s_memrealtime(); PG8_WAIT_V(8); pg8_probe_acc += (unsigned)(__builtin_amdgcn_s_memrealtime() - tq_); }
;     ...
;             PG8_WAIT_V(8); PG8_WAIT_L(0); PG8_BAR; PG8_MMA(0, 0, At, B0); PG8_MMA(0, 1, At, B1); PG8_BAR; PG8_SCHED;
;             PG8_LDA(At, 0, 1); PG8_STAGE(PG8_SB(0, 0), b2, voffB); PG8_STAGE(PG8_SB(0, 1), b2 + hstep, voffB); PG8_STAGE(PG8_SA(0, 0), a2, voffA);
;             PG8_WAIT_V(8); PG8_WAIT_L(0); PG8_BAR; if (cur.half == 0) { PG8_MMA(1, 0, At, B0); PG8_MMA(1, 1, At, B1); } PG8_BAR; PG8_SCHED;
;             PG8_LDB(B0, 1, 0); PG8_LDB(B1, 1, 1); PG8_SCHED; PG8_LDA(At, 1, 0); PG8_STAGE(PG8_SA(0, 1), a2 + hstep, voffA);
;             PG8_WAIT_V(8); PG8_WAIT_L(0); PG8_BAR; PG8_MMA(0, 0, At, B0); PG8_MMA(0, 1, At, B1); PG8_BAR; PG8_SCHED;
;             PG8_LDA(At, 1, 1); PG8_STAGE(PG8_SB(1, 0), b3, voffB); PG8_STAGE(PG8_SB(1, 1), b3 + hstep, voffB); PG8_STAGE(PG8_SA(1, 0), a3, voffA);
;             PG8_WAIT_V(8); PG8_WAIT_L(0); PG8_BAR; if (cur.half == 0) { PG8_MMA(1, 0, At, B0); PG8_MMA(1, 1, At, B1); } PG8_BAR; PG8_SCHED;
	s_add_i32 s10, s61, s27
	v_lshl_add_u64 v[228:229], v[228:229], 0, s[42:43]
	s_mov_b32 m0, s10
	ds_read_b128 v[182:185], v206 offset:49152
	ds_read_b128 v[186:189], v206 offset:50176
	ds_read_b128 v[190:193], v206 offset:51200
	ds_read_b128 v[194:197], v206 offset:52224
	ds_read_b128 v[198:201], v206 offset:53248
	ds_read_b128 v[208:211], v206 offset:54272
	ds_read_b128 v[212:215], v206 offset:55296
	ds_read_b128 v[216:219], v206 offset:56320
	global_load_lds_dwordx4 v[228:229], off
	s_add_i32 m0, s10, 0x2000
	s_add_u32 s0, s0, 0x40080
	v_lshl_add_u64 v[228:229], v[230:231], 0, s[42:43]
	s_addc_u32 s1, s1, 0
	s_add_i32 s10, s63, s27
	global_load_lds_dwordx4 v[228:229], off
	v_lshl_add_u64 v[228:229], s[0:1], 0, v[166:167]
	s_mov_b32 m0, s10
	s_nop 0
	global_load_lds_dwordx4 v[228:229], off
	v_lshl_add_u64 v[228:229], s[0:1], 0, v[170:171]
	s_add_i32 m0, s10, 0x2000
	s_nop 0
	global_load_lds_dwordx4 v[228:229], off
	v_lshl_add_u64 v[228:229], v[232:233], 0, s[42:43]
	s_mov_b32 m0, s41
	s_nop 0
	global_load_lds_dwordx4 v[228:229], off
	v_lshl_add_u64 v[228:229], v[234:235], 0, s[42:43]
	s_mov_b32 m0, s71
	s_nop 0
	global_load_lds_dwordx4 v[228:229], off
	s_waitcnt vmcnt(8)
	s_waitcnt lgkmcnt(0)
	s_barrier
	s_setprio 1
	s_waitcnt lgkmcnt(0)
	v_mfma_f32_16x16x32_bf16 v[64:67], v[132:135], v[182:185], v[64:67]
	v_mfma_f32_16x16x32_bf16 v[60:63], v[140:143], v[182:185], v[60:63]
	v_mfma_f32_16x16x32_bf16 v[48:51], v[132:135], v[190:193], v[48:51]
	v_mfma_f32_16x16x32_bf16 v[44:47], v[140:143], v[190:193], v[44:47]
	v_mfma_f32_16x16x32_bf16 v[32:35], v[132:135], v[198:201], v[32:35]
	v_mfma_f32_16x16x32_bf16 v[28:31], v[140:143], v[198:201], v[28:31]
	v_mfma_f32_16x16x32_bf16 v[16:19], v[132:135], v[212:215], v[16:19]
	v_mfma_f32_16x16x32_bf16 v[12:15], v[140:143], v[212:215], v[12:15]
	v_mfma_f32_16x16x32_bf16 v[64:67], v[136:139], v[186:189], v[64:67]
	v_mfma_f32_16x16x32_bf16 v[60:63], v[144:147], v[186:189], v[60:63]
	v_mfma_f32_16x16x32_bf16 v[48:51], v[136:139], v[194:197], v[48:51]
	v_mfma_f32_16x16x32_bf16 v[44:47], v[144:147], v[194:197], v[44:47]
	v_mfma_f32_16x16x32_bf16 v[32:35], v[136:139], v[208:211], v[32:35]
	v_mfma_f32_16x16x32_bf16 v[28:31], v[144:147], v[208:211], v[28:31]
	v_mfma_f32_16x16x32_bf16 v[16:19], v[136:139], v[216:219], v[16:19]
	v_mfma_f32_16x16x32_bf16 v[12:15], v[144:147], v[216:219], v[12:15]
	s_setprio 0
	s_setprio 1
	v_mfma_f32_16x16x32_bf16 v[56:59], v[148:151], v[182:185], v[56:59]
	v_mfma_f32_16x16x32_bf16 v[52:55], v[156:159], v[182:185], v[52:55]
	v_mfma_f32_16x16x32_bf16 v[40:43], v[148:151], v[190:193], v[40:43]
	v_mfma_f32_16x16x32_bf16 v[36:39], v[156:159], v[190:193], v[36:39]
	v_mfma_f32_16x16x32_bf16 v[24:27], v[148:151], v[198:201], v[24:27]
	v_mfma_f32_16x16x32_bf16 v[20:23], v[156:159], v[198:201], v[20:23]
	v_mfma_f32_16x16x32_bf16 v[8:11], v[148:151], v[212:215], v[8:11]
	v_mfma_f32_16x16x32_bf16 v[4:7], v[156:159], v[212:215], v[4:7]
	v_mfma_f32_16x16x32_bf16 v[56:59], v[152:155], v[186:189], v[56:59]
	v_mfma_f32_16x16x32_bf16 v[52:55], v[160:163], v[186:189], v[52:55]
	v_mfma_f32_16x16x32_bf16 v[40:43], v[152:155], v[194:197], v[40:43]
	v_mfma_f32_16x16x32_bf16 v[36:39], v[160:163], v[194:197], v[36:39]
	v_mfma_f32_16x16x32_bf16 v[24:27], v[152:155], v[208:211], v[24:27]
	v_mfma_f32_16x16x32_bf16 v[20:23], v[160:163], v[208:211], v[20:23]
	v_mfma_f32_16x16x32_bf16 v[8:11], v[152:155], v[216:219], v[8:11]
	v_mfma_f32_16x16x32_bf16 v[4:7], v[160:163], v[216:219], v[4:7]
	s_setprio 0
	s_barrier
	s_add_i32 s39, s39, 2
	s_add_u32 s8, s8, 0x100
	s_addc_u32 s9, s9, 0
	s_add_u32 s36, s36, 0x100
	s_addc_u32 s38, s38, 0
	s_mov_b32 s32, 1
	.p2align 6

;     __device__ bool next(int i, Unit& u) const { if (!base.next(i >> 1, u)) return false; if (i & 1) { u.pm += MTOK / BM; u.pn += DM / BM; } return true; }
;   __device__ __forceinline__ bool next(int i,AttnUnit&u)const{ if(i>=2||vcu>=256)return false; const int s=vcu&3; u.bh=vcu>>2; u.qb=(i==0)?7-s:s; return true; }
; template <class Epi, class Sched, bool ALIGN_EPI = false, bool SP2 = false>
; __device__ __forceinline__ void gemm_phase(PG8_LAS unsigned char* lds, const Gemm g, const Sched& S, const Epi& E) {
;     ...
;     for (;;) {
;         const bool has_next = S.next(ui + 1, nxt);
;         const char* nA = has_next ? (const char*)g.A + (size_t)nxt.pm * tstep + (nxt.half == 2 ? hstep : (size_t)0) : cA; const char* nB = has_next ? (const char*)g.Bt + (size_t)nxt.pn * tstep : cB;
;         for (int t = 0; t < nt; t += 2) {
;             const bool last = (t == nt - 2);
;             const char* a1 = cA + (size_t)(t + 1) * kstep;
;             const char* a2 = last ? nA : cA + (size_t)(t + 2) * kstep; const char* b2 = last ? nB : cB + (size_t)(t + 2) * kstep;
;             const char* a3 = a2 + kstep; const char* b3 = b2 + kstep;
.LBB0_1134:
	s_bitcmp0_b32 s1, 0
	s_cselect_b64 s[20:21], -1, 0
	s_and_b64 s[20:21], s[20:21], s[60:61]
	s_add_i32 s1, s18, 64
	s_add_i32 s5, s38, 4
	s_and_b64 s[20:21], s[20:21], exec
	s_cselect_b32 s18, s1, s18
	s_cselect_b32 s38, s5, s38
	s_ashr_i32 s19, s18, 31
	s_lshl_b64 s[20:21], s[18:19], 18
	s_add_u32 s56, s23, s20
	s_addc_u32 s57, s24, s21
	s_and_b64 s[20:21], s[60:61], exec
	s_cselect_b32 s1, s57, s7
	s_cselect_b32 s5, s56, s6
	s_ashr_i32 s39, s38, 31
	s_lshl_b64 s[20:21], s[38:39], 18
	s_add_u32 s58, s25, s20
	s_addc_u32 s59, s26, s21
	s_and_b64 s[20:21], s[60:61], exec
	s_cselect_b32 s19, s59, s15
	s_cselect_b32 s39, s58, s14
	s_add_u32 s6, s6, 0x20080
	s_addc_u32 s7, s7, 0
	s_add_u32 s62, s14, 0x100
	s_addc_u32 s63, s15, 0
	s_mov_b32 s64, -2
	.p2align 6

;     __device__ bool next(int i, Unit& u) const { if (!base.next(i >> 1, u)) return false; if (i & 1) { u.pm += MTOK / BM; u.pn += DM / BM; } return true; }
;   __device__ __forceinline__ bool next(int i,AttnUnit&u)const{ if(i>=2||vcu>=256)return false; const int s=vcu&3; u.bh=vcu>>2; u.qb=(i==0)?7-s:s; return true; }
; template <class Epi, class Sched, bool ALIGN_EPI = false, bool SP2 = false>
; __device__ __forceinline__ void gemm_phase(PG8_LAS unsigned char* lds, const Gemm g, const Sched& S, const Epi& E) {
;     ...
;     for (;;) {
;         const bool has_next = S.next(ui + 1, nxt);
;         const char* nA = has_next ? (const char*)g.A + (size_t)nxt.pm * tstep + (nxt.half == 2 ? hstep : (size_t)0) : cA; const char* nB = has_next ? (const char*)g.Bt + (size_t)nxt.pn * tstep : cB;
;         for (int t = 0; t < nt; t += 2) {
;             const bool last = (t == nt - 2);
;             const char* a1 = cA + (size_t)(t + 1) * kstep;
;             const char* a2 = last ? nA : cA + (size_t)(t + 2) * kstep; const char* b2 = last ? nB : cB + (size_t)(t + 2) * kstep;
;             const char* a3 = a2 + kstep; const char* b3 = b2 + kstep;
.LBB0_1299:
	s_add_u32 s62, s0, 0x100
	s_addc_u32 s63, s1, 0
	s_ashr_i32 s7, s6, 31
	s_lshl_b64 s[18:19], s[6:7], 19
	s_add_u32 s26, s34, s18
	s_addc_u32 s27, s35, s19
	s_and_b64 s[18:19], s[20:21], exec
	s_cselect_b32 s7, s27, s5
	s_cselect_b32 s64, s26, s4
	s_ashr_i32 s11, s10, 31
	s_lshl_b64 s[18:19], s[10:11], 19
	s_add_u32 s18, s36, s18
	s_addc_u32 s19, s38, s19
	s_and_b64 s[28:29], s[20:21], exec
	s_cselect_b32 s11, s19, s1
	s_cselect_b32 s65, s18, s0
	s_add_u32 s0, s4, 0x40080
	s_addc_u32 s1, s5, 0
	v_lshl_add_u64 v[142:143], s[0:1], 0, v[138:139]
	v_lshl_add_u64 v[144:145], s[0:1], 0, v[140:141]
	s_mov_b32 s66, -2
	s_mov_b64 s[0:1], 0
	.p2align 6

; #define PG8_STAGE(bufoff, gbase, voff) do { _Pragma("unroll") for (int _i = 0; _i < 2; ++_i) \
;         __builtin_amdgcn_global_load_lds((const unsigned*)((const char*)(gbase) + (voff)[_i]), (PG8_LAS unsigned*)(lds + (bufoff) + ldsw + _i * 8192), 16, 0, 0); } while (0)
; #define PG8_LDA(dst, b, h) do { _Pragma("unroll") for (int m = 0; m < 4; ++m) _Pragma("unroll") for (int k = 0; k < 2; ++k) dst[m][k] = *(const PG8_LAS bf16x8*)(lds + PG8_SA(b, h) + aoff + m * 2048 + k * 1024); } while (0)
; #define PG8_LDB(dst, b, h) do { _Pragma("unroll") for (int n = 0; n < 2; ++n) _Pragma("unroll") for (int k = 0; k < 2; ++k) dst[n][k] = *(const PG8_LAS bf16x8*)(lds + PG8_SB(b, h) + boff + n * 2048 + k * 1024); } while (0)
; #define PG8_WAIT_V(n) asm volatile("s_waitcnt vmcnt(" #n ")" ::: "memory")
; #define PG8_WAIT_L(n) asm volatile("s_waitcnt lgkmcnt(" #n ")" ::: "memory")
; template <class Epi, class Sched, bool ALIGN_EPI = false, bool SP2 = false>
; __device__ __forceinline__ void gemm_phase(PG8_LAS unsigned char* lds, const Gemm g, const Sched& S, const Epi& E) {
;     ...
;             PG8_LDB(B0, 0, 0); PG8_LDB(B1, 0, 1); PG8_SCHED; PG8_LDA(At, 0, 0); PG8_STAGE(PG8_SA(1, 1), a1 + hstep, voffA);
;     ...
;             if (PROBE_KIND == 18 && t == 0 && ui > 0 && g.probe) { const unsigned long long tq_ = __builtin_amdgcn_s_memrealtime(); PG8_WAIT_V(8); pg8_probe_acc += (unsigned)(__builtin_amdgcn_s_memrealtime() - tq_); }
;     ...
;             PG8_WAIT_V(8); PG8_WAIT_L(0); PG8_BAR; PG8_MMA(0, 0, At, B0); PG8_MMA(0, 1, At, B1); PG8_BAR; PG8_SCHED;
;             PG8_LDA(At, 0, 1); PG8_STAGE(PG8_SB(0, 0), b2, voffB); PG8_STAGE(PG8_SB(0, 1), b2 + hstep, voffB); PG8_STAGE(PG8_SA(0, 0), a2, voffA);
;             PG8_WAIT_V(8); PG8_WAIT_L(0); PG8_BAR; if (cur.half == 0) { PG8_MMA(1, 0, At, B0); PG8_MMA(1, 1, At, B1); } PG8_BAR; PG8_SCHED;
;             PG8_LDB(B0, 1, 0); PG8_LDB(B1, 1, 1); PG8_SCHED; PG8_LDA(At, 1, 0); PG8_STAGE(PG8_SA(0, 1), a2 + hstep, voffA);
;             PG8_WAIT_V(8); PG8_WAIT_L(0); PG8_BAR; PG8_MMA(0, 0, At, B0); PG8_MMA(0, 1, At, B1); PG8_BAR; PG8_SCHED;
;             PG8_LDA(At, 1, 1); PG8_STAGE(PG8_SB(1, 0), b3, voffB); PG8_STAGE(PG8_SB(1, 1), b3 + hstep, voffB); PG8_STAGE(PG8_SA(1, 0), a3, voffA);
;             PG8_WAIT_V(8); PG8_WAIT_L(0); PG8_BAR; if (cur.half == 0) { PG8_MMA(1, 0, At, B0); PG8_MMA(1, 1, At, B1); } PG8_BAR; PG8_SCHED;
.Lpj_gu_2:
	s_waitcnt lgkmcnt(0)
	s_barrier
	s_setprio 1
	s_waitcnt lgkmcnt(0)
	v_mfma_f32_16x16x32_bf16 v[64:67], v[142:145], v[180:183], 0
	v_mfma_f32_16x16x32_bf16 v[60:63], v[156:159], v[180:183], 0
	v_mfma_f32_16x16x32_bf16 v[48:51], v[142:145], v[188:191], 0
	v_mfma_f32_16x16x32_bf16 v[44:47], v[156:159], v[188:191], 0
	v_mfma_f32_16x16x32_bf16 v[32:35], v[142:145], v[196:199], 0
	v_mfma_f32_16x16x32_bf16 v[28:31], v[156:159], v[196:199], 0
	v_mfma_f32_16x16x32_bf16 v[16:19], v[142:145], v[204:207], 0
	v_mfma_f32_16x16x32_bf16 v[12:15], v[156:159], v[204:207], 0
	v_mfma_f32_16x16x32_bf16 v[64:67], v[152:155], v[184:187], v[64:67]
	v_mfma_f32_16x16x32_bf16 v[60:63], v[160:163], v[184:187], v[60:63]
	v_mfma_f32_16x16x32_bf16 v[48:51], v[152:155], v[192:195], v[48:51]
	v_mfma_f32_16x16x32_bf16 v[44:47], v[160:163], v[192:195], v[44:47]
	v_mfma_f32_16x16x32_bf16 v[32:35], v[152:155], v[200:203], v[32:35]
	v_mfma_f32_16x16x32_bf16 v[28:31], v[160:163], v[200:203], v[28:31]
	v_mfma_f32_16x16x32_bf16 v[16:19], v[152:155], v[208:211], v[16:19]
	v_mfma_f32_16x16x32_bf16 v[12:15], v[160:163], v[208:211], v[12:15]
	s_setprio 0
	s_setprio 1
	v_mfma_f32_16x16x32_bf16 v[56:59], v[164:167], v[180:183], 0
	v_mfma_f32_16x16x32_bf16 v[52:55], v[172:175], v[180:183], 0
	v_mfma_f32_16x16x32_bf16 v[40:43], v[164:167], v[188:191], 0
	v_mfma_f32_16x16x32_bf16 v[36:39], v[172:175], v[188:191], 0
	v_mfma_f32_16x16x32_bf16 v[24:27], v[164:167], v[196:199], 0
	v_mfma_f32_16x16x32_bf16 v[20:23], v[172:175], v[196:199], 0
	v_mfma_f32_16x16x32_bf16 v[8:11], v[164:167], v[204:207], 0
	v_mfma_f32_16x16x32_bf16 v[4:7], v[172:175], v[204:207], 0
	v_mfma_f32_16x16x32_bf16 v[56:59], v[168:171], v[184:187], v[56:59]
	v_mfma_f32_16x16x32_bf16 v[52:55], v[176:179], v[184:187], v[52:55]
	v_mfma_f32_16x16x32_bf16 v[40:43], v[168:171], v[192:195], v[40:43]
	v_mfma_f32_16x16x32_bf16 v[36:39], v[176:179], v[192:195], v[36:39]
	v_mfma_f32_16x16x32_bf16 v[24:27], v[168:171], v[200:203], v[24:27]
	v_mfma_f32_16x16x32_bf16 v[20:23], v[176:179], v[200:203], v[20:23]
	v_mfma_f32_16x16x32_bf16 v[8:11], v[168:171], v[208:211], v[8:11]
	v_mfma_f32_16x16x32_bf16 v[4:7], v[176:179], v[208:211], v[4:7]
	s_setprio 0
	s_barrier
	s_add_i32 s67, 0, 0x18000
	v_add_u32_e32 v151, s67, v147
	s_add_i32 s68, 0, 0x1c000
	ds_read_b128 v[142:145], v151
	ds_read_b128 v[152:155], v151 offset:1024
	ds_read_b128 v[156:159], v151 offset:2048
	ds_read_b128 v[160:163], v151 offset:3072
	v_add_u32_e32 v151, s68, v147
	ds_read_b128 v[164:167], v151
	ds_read_b128 v[168:171], v151 offset:1024
	ds_read_b128 v[172:175], v151 offset:2048
	ds_read_b128 v[176:179], v151 offset:3072
	s_add_u32 s28, s28, 0x40000
	s_addc_u32 s29, s29, 0
	s_mov_b32 m0, s36
	v_lshl_add_u64 v[220:221], s[28:29], 0, v[132:133]
	ds_read_b128 v[180:183], v150 offset:32768
	ds_read_b128 v[184:187], v150 offset:33792
	ds_read_b128 v[188:191], v150 offset:34816
	ds_read_b128 v[192:195], v150 offset:35840
	ds_read_b128 v[196:199], v150 offset:36864
	ds_read_b128 v[200:203], v150 offset:37888
	ds_read_b128 v[204:207], v150 offset:38912
	ds_read_b128 v[208:211], v150 offset:39936
	global_load_lds_dwordx4 v[220:221], off
	v_lshl_add_u64 v[220:221], s[28:29], 0, v[134:135]
	s_mov_b32 m0, s40
	s_nop 0
	global_load_lds_dwordx4 v[220:221], off
	s_waitcnt vmcnt(8)
	s_waitcnt lgkmcnt(0)
	s_barrier
	s_setprio 1
	s_waitcnt lgkmcnt(0)
	v_mfma_f32_16x16x32_bf16 v[128:131], v[142:145], v[180:183], v[128:131]
	v_mfma_f32_16x16x32_bf16 v[124:127], v[156:159], v[180:183], v[124:127]
	v_mfma_f32_16x16x32_bf16 v[112:115], v[142:145], v[188:191], v[112:115]
	v_mfma_f32_16x16x32_bf16 v[108:111], v[156:159], v[188:191], v[108:111]
	v_mfma_f32_16x16x32_bf16 v[96:99], v[142:145], v[196:199], v[96:99]
	v_mfma_f32_16x16x32_bf16 v[92:95], v[156:159], v[196:199], v[92:95]
	v_mfma_f32_16x16x32_bf16 v[80:83], v[142:145], v[204:207], v[80:83]
	v_mfma_f32_16x16x32_bf16 v[76:79], v[156:159], v[204:207], v[76:79]
	v_mfma_f32_16x16x32_bf16 v[128:131], v[152:155], v[184:187], v[128:131]
	v_mfma_f32_16x16x32_bf16 v[124:127], v[160:163], v[184:187], v[124:127]
	v_mfma_f32_16x16x32_bf16 v[112:115], v[152:155], v[192:195], v[112:115]
	v_mfma_f32_16x16x32_bf16 v[108:111], v[160:163], v[192:195], v[108:111]
	v_mfma_f32_16x16x32_bf16 v[96:99], v[152:155], v[200:203], v[96:99]
	v_mfma_f32_16x16x32_bf16 v[92:95], v[160:163], v[200:203], v[92:95]
	v_mfma_f32_16x16x32_bf16 v[80:83], v[152:155], v[208:211], v[80:83]
	v_mfma_f32_16x16x32_bf16 v[76:79], v[160:163], v[208:211], v[76:79]
	s_setprio 0
	s_setprio 1
	v_mfma_f32_16x16x32_bf16 v[120:123], v[164:167], v[180:183], v[120:123]
	v_mfma_f32_16x16x32_bf16 v[116:119], v[172:175], v[180:183], v[116:119]
	v_mfma_f32_16x16x32_bf16 v[104:107], v[164:167], v[188:191], v[104:107]
	v_mfma_f32_16x16x32_bf16 v[100:103], v[172:175], v[188:191], v[100:103]
	v_mfma_f32_16x16x32_bf16 v[88:91], v[164:167], v[196:199], v[88:91]
	v_mfma_f32_16x16x32_bf16 v[84:87], v[172:175], v[196:199], v[84:87]
	v_mfma_f32_16x16x32_bf16 v[72:75], v[164:167], v[204:207], v[72:75]
	v_mfma_f32_16x16x32_bf16 v[68:71], v[172:175], v[204:207], v[68:71]
	v_mfma_f32_16x16x32_bf16 v[120:123], v[168:171], v[184:187], v[120:123]
	v_mfma_f32_16x16x32_bf16 v[116:119], v[176:179], v[184:187], v[116:119]
	v_mfma_f32_16x16x32_bf16 v[104:107], v[168:171], v[192:195], v[104:107]
	v_mfma_f32_16x16x32_bf16 v[100:103], v[176:179], v[192:195], v[100:103]
	v_mfma_f32_16x16x32_bf16 v[88:91], v[168:171], v[200:203], v[88:91]
	v_mfma_f32_16x16x32_bf16 v[84:87], v[176:179], v[200:203], v[84:87]
	v_mfma_f32_16x16x32_bf16 v[72:75], v[168:171], v[208:211], v[72:75]
	v_mfma_f32_16x16x32_bf16 v[68:71], v[176:179], v[208:211], v[68:71]
	s_setprio 0
	s_barrier
; #define PG8_STAGE(bufoff, gbase, voff) do { _Pragma("unroll") for (int _i = 0; _i < 2; ++_i) \
;         __builtin_amdgcn_global_load_lds((const unsigned*)((const char*)(gbase) + (voff)[_i]), (PG8_LAS unsigned*)(lds + (bufoff) + ldsw + _i * 8192), 16, 0, 0); } while (0)
; #define PG8_LDA(dst, b, h) do { _Pragma("unroll") for (int m = 0; m < 4; ++m) _Pragma("unroll") for (int k = 0; k < 2; ++k) dst[m][k] = *(const PG8_LAS bf16x8*)(lds + PG8_SA(b, h) + aoff + m * 2048 + k * 1024); } while (0)
; #define PG8_LDB(dst, b, h) do { _Pragma("unroll") for (int n = 0; n < 2; ++n) _Pragma("unroll") for (int k = 0; k < 2; ++k) dst[n][k] = *(const PG8_LAS bf16x8*)(lds + PG8_SB(b, h) + boff + n * 2048 + k * 1024); } while (0)
; #define PG8_WAIT_V(n) asm volatile("s_waitcnt vmcnt(" #n ")" ::: "memory")
; #define PG8_WAIT_L(n) asm volatile("s_waitcnt lgkmcnt(" #n ")" ::: "memory")
; template <class Epi, class Sched, bool ALIGN_EPI = false, bool SP2 = false>
; __device__ __forceinline__ void gemm_phase(PG8_LAS unsigned char* lds, const Gemm g, const Sched& S, const Epi& E) {
;     ...
;             PG8_LDB(B0, 0, 0); PG8_LDB(B1, 0, 1); PG8_SCHED; PG8_LDA(At, 0, 0); PG8_STAGE(PG8_SA(1, 1), a1 + hstep, voffA);
;     ...
;             if (PROBE_KIND == 18 && t == 0 && ui > 0 && g.probe) { const unsigned long long tq_ = __builtin_amdgcn_s_memrealtime(); PG8_WAIT_V(8); pg8_probe_acc += (unsigned)(__builtin_amdgcn_s_memrealtime() - tq_); }
;     ...
;             PG8_WAIT_V(8); PG8_WAIT_L(0); PG8_BAR; PG8_MMA(0, 0, At, B0); PG8_MMA(0, 1, At, B1); PG8_BAR; PG8_SCHED;
;             PG8_LDA(At, 0, 1); PG8_STAGE(PG8_SB(0, 0), b2, voffB); PG8_STAGE(PG8_SB(0, 1), b2 + hstep, voffB); PG8_STAGE(PG8_SA(0, 0), a2, voffA);
;             PG8_WAIT_V(8); PG8_WAIT_L(0); PG8_BAR; if (cur.half == 0) { PG8_MMA(1, 0, At, B0); PG8_MMA(1, 1, At, B1); } PG8_BAR; PG8_SCHED;
;             PG8_LDB(B0, 1, 0); PG8_LDB(B1, 1, 1); PG8_SCHED; PG8_LDA(At, 1, 0); PG8_STAGE(PG8_SA(0, 1), a2 + hstep, voffA);
;             PG8_WAIT_V(8); PG8_WAIT_L(0); PG8_BAR; PG8_MMA(0, 0, At, B0); PG8_MMA(0, 1, At, B1); PG8_BAR; PG8_SCHED;
;             PG8_LDA(At, 1, 1); PG8_STAGE(PG8_SB(1, 0), b3, voffB); PG8_STAGE(PG8_SB(1, 1), b3 + hstep, voffB); PG8_STAGE(PG8_SA(1, 0), a3, voffA);
;             PG8_WAIT_V(8); PG8_WAIT_L(0); PG8_BAR; if (cur.half == 0) { PG8_MMA(1, 0, At, B0); PG8_MMA(1, 1, At, B1); } PG8_BAR; PG8_SCHED;
	s_add_i32 s28, s67, s25
	v_lshl_add_u64 v[212:213], v[212:213], 0, s[42:43]
	s_mov_b32 m0, s28
	ds_read_b128 v[180:183], v150 offset:49152
	ds_read_b128 v[184:187], v150 offset:50176
	ds_read_b128 v[188:191], v150 offset:51200
	ds_read_b128 v[192:195], v150 offset:52224
	ds_read_b128 v[196:199], v150 offset:53248
	ds_read_b128 v[200:203], v150 offset:54272
	ds_read_b128 v[204:207], v150 offset:55296
	ds_read_b128 v[208:211], v150 offset:56320
	global_load_lds_dwordx4 v[212:213], off
	s_add_i32 m0, s28, 0x2000
	s_add_u32 s0, s0, 0x40080
	v_lshl_add_u64 v[212:213], v[214:215], 0, s[42:43]
	s_addc_u32 s1, s1, 0
	s_add_i32 s28, s68, s25
	global_load_lds_dwordx4 v[212:213], off
	v_lshl_add_u64 v[212:213], s[0:1], 0, v[2:3]
	s_mov_b32 m0, s28
	s_nop 0
	global_load_lds_dwordx4 v[212:213], off
	v_lshl_add_u64 v[212:213], s[0:1], 0, v[136:137]
	s_add_i32 m0, s28, 0x2000
	s_nop 0
	global_load_lds_dwordx4 v[212:213], off
	v_lshl_add_u64 v[212:213], v[216:217], 0, s[42:43]
	s_mov_b32 m0, s41
	s_nop 0
	global_load_lds_dwordx4 v[212:213], off
	v_lshl_add_u64 v[212:213], v[218:219], 0, s[42:43]
	s_mov_b32 m0, s60
	s_nop 0
	global_load_lds_dwordx4 v[212:213], off
	s_waitcnt vmcnt(8)
	s_waitcnt lgkmcnt(0)
	s_barrier
	s_setprio 1
	s_waitcnt lgkmcnt(0)
	v_mfma_f32_16x16x32_bf16 v[64:67], v[142:145], v[180:183], v[64:67]
	v_mfma_f32_16x16x32_bf16 v[60:63], v[156:159], v[180:183], v[60:63]
	v_mfma_f32_16x16x32_bf16 v[48:51], v[142:145], v[188:191], v[48:51]
	v_mfma_f32_16x16x32_bf16 v[44:47], v[156:159], v[188:191], v[44:47]
	v_mfma_f32_16x16x32_bf16 v[32:35], v[142:145], v[196:199], v[32:35]
	v_mfma_f32_16x16x32_bf16 v[28:31], v[156:159], v[196:199], v[28:31]
	v_mfma_f32_16x16x32_bf16 v[16:19], v[142:145], v[204:207], v[16:19]
	v_mfma_f32_16x16x32_bf16 v[12:15], v[156:159], v[204:207], v[12:15]
	v_mfma_f32_16x16x32_bf16 v[64:67], v[152:155], v[184:187], v[64:67]
	v_mfma_f32_16x16x32_bf16 v[60:63], v[160:163], v[184:187], v[60:63]
	v_mfma_f32_16x16x32_bf16 v[48:51], v[152:155], v[192:195], v[48:51]
	v_mfma_f32_16x16x32_bf16 v[44:47], v[160:163], v[192:195], v[44:47]
	v_mfma_f32_16x16x32_bf16 v[32:35], v[152:155], v[200:203], v[32:35]
	v_mfma_f32_16x16x32_bf16 v[28:31], v[160:163], v[200:203], v[28:31]
	v_mfma_f32_16x16x32_bf16 v[16:19], v[152:155], v[208:211], v[16:19]
	v_mfma_f32_16x16x32_bf16 v[12:15], v[160:163], v[208:211], v[12:15]
	s_setprio 0
	s_setprio 1
	v_mfma_f32_16x16x32_bf16 v[56:59], v[164:167], v[180:183], v[56:59]
	v_mfma_f32_16x16x32_bf16 v[52:55], v[172:175], v[180:183], v[52:55]
	v_mfma_f32_16x16x32_bf16 v[40:43], v[164:167], v[188:191], v[40:43]
	v_mfma_f32_16x16x32_bf16 v[36:39], v[172:175], v[188:191], v[36:39]
	v_mfma_f32_16x16x32_bf16 v[24:27], v[164:167], v[196:199], v[24:27]
	v_mfma_f32_16x16x32_bf16 v[20:23], v[172:175], v[196:199], v[20:23]
	v_mfma_f32_16x16x32_bf16 v[8:11], v[164:167], v[204:207], v[8:11]
	v_mfma_f32_16x16x32_bf16 v[4:7], v[172:175], v[204:207], v[4:7]
	v_mfma_f32_16x16x32_bf16 v[56:59], v[168:171], v[184:187], v[56:59]
	v_mfma_f32_16x16x32_bf16 v[52:55], v[176:179], v[184:187], v[52:55]
	v_mfma_f32_16x16x32_bf16 v[40:43], v[168:171], v[192:195], v[40:43]
	v_mfma_f32_16x16x32_bf16 v[36:39], v[176:179], v[192:195], v[36:39]
	v_mfma_f32_16x16x32_bf16 v[24:27], v[168:171], v[200:203], v[24:27]
	v_mfma_f32_16x16x32_bf16 v[20:23], v[176:179], v[200:203], v[20:23]
	v_mfma_f32_16x16x32_bf16 v[8:11], v[168:171], v[208:211], v[8:11]
	v_mfma_f32_16x16x32_bf16 v[4:7], v[176:179], v[208:211], v[4:7]
	s_setprio 0
	s_barrier
	s_add_i32 s66, s66, 2
	s_add_u32 s26, s26, 0x100
	s_addc_u32 s27, s27, 0
	s_add_u32 s64, s64, 0x100
	s_addc_u32 s65, s65, 0
	s_mov_b32 s32, 1
	.p2align 6

;     __device__ bool next(int i, Unit& u) const { if (!base.next(i >> 1, u)) return false; if (i & 1) { u.pm += MTOK / BM; u.pn += DM / BM; } return true; }
;   __device__ __forceinline__ bool next(int i,AttnUnit&u)const{ if(i>=2||vcu>=256)return false; const int s=vcu&3; u.bh=vcu>>2; u.qb=(i==0)?7-s:s; return true; }
; template <class Epi, class Sched, bool ALIGN_EPI = false, bool SP2 = false>
; __device__ __forceinline__ void gemm_phase(PG8_LAS unsigned char* lds, const Gemm g, const Sched& S, const Epi& E) {
;     ...
;     for (;;) {
;         const bool has_next = S.next(ui + 1, nxt);
;         const char* nA = has_next ? (const char*)g.A + (size_t)nxt.pm * tstep + (nxt.half == 2 ? hstep : (size_t)0) : cA; const char* nB = has_next ? (const char*)g.Bt + (size_t)nxt.pn * tstep : cB;
;         for (int t = 0; t < nt; t += 2) {
;             const bool last = (t == nt - 2);
;             const char* a1 = cA + (size_t)(t + 1) * kstep;
;             const char* a2 = last ? nA : cA + (size_t)(t + 2) * kstep; const char* b2 = last ? nB : cB + (size_t)(t + 2) * kstep;
;             const char* a3 = a2 + kstep; const char* b3 = b2 + kstep;
.LBB0_1779:
	s_add_u32 s60, s0, 0x100
	s_addc_u32 s61, s1, 0
	s_add_u32 s0, s6, 0xb0080
	s_addc_u32 s1, s7, 0
	v_lshl_add_u64 v[142:143], s[0:1], 0, v[138:139]
	v_lshl_add_u64 v[144:145], s[0:1], 0, v[140:141]
	s_mov_b32 s62, -2
	s_mov_b64 s[0:1], 0
	.p2align 6
